# P2 gate tiles: LDS table look-ups software-pipelined over two index register sets, 3-op byte packing (on top of v68)
# baseline (speedup 1.0000x reference)
.LBB0_327:
	s_cmp_gt_i32 s0, 10
	s_mov_b64 s[10:11], -1
	s_cbranch_scc0 .LBB0_329
	v_ashrrev_i32_e32 v169, 31, v168
	v_lshlrev_b64 v[130:131], 11, v[168:169]
	v_lshl_add_u32 v146, s0, 8, v195
	v_lshl_add_u64 v[130:131], s[76:77], 0, v[130:131]
	v_lshl_add_u64 v[130:131], v[130:131], 0, v[146:147]
	v_fmamk_f32 v132, v126, 0x43000000, v198
	v_fmamk_f32 v133, v127, 0x43000000, v198
	v_fmamk_f32 v134, v128, 0x43000000, v198
	v_fmamk_f32 v135, v129, 0x43000000, v198
	v_fmamk_f32 v136, v122, 0x43000000, v198
	v_fmamk_f32 v137, v123, 0x43000000, v198
	v_fmamk_f32 v169, v124, 0x43000000, v198
	v_fmamk_f32 v170, v125, 0x43000000, v198
	v_med3_f32 v132, v132, s69, v199
	v_med3_f32 v133, v133, s69, v199
	v_med3_f32 v134, v134, s69, v199
	v_med3_f32 v135, v135, s69, v199
	v_med3_f32 v136, v136, s69, v199
	v_med3_f32 v137, v137, s69, v199
	v_med3_f32 v169, v169, s69, v199
	v_med3_f32 v170, v170, s69, v199
	v_cvt_i32_f32_e32 v132, v132
	v_cvt_i32_f32_e32 v133, v133
	v_cvt_i32_f32_e32 v134, v134
	v_cvt_i32_f32_e32 v135, v135
	v_cvt_i32_f32_e32 v136, v136
	v_cvt_i32_f32_e32 v137, v137
	v_cvt_i32_f32_e32 v169, v169
	v_cvt_i32_f32_e32 v170, v170
	ds_read_u8 v132, v132
	ds_read_u8 v133, v133
	ds_read_u8 v134, v134
	ds_read_u8 v135, v135
	ds_read_u8 v136, v136
	ds_read_u8 v137, v137
	ds_read_u8 v169, v169
	ds_read_u8 v170, v170
	v_fmamk_f32 v180, v118, 0x43000000, v198
	v_fmamk_f32 v181, v119, 0x43000000, v198
	v_fmamk_f32 v182, v120, 0x43000000, v198
	v_fmamk_f32 v183, v121, 0x43000000, v198
	v_fmamk_f32 v184, v114, 0x43000000, v198
	v_fmamk_f32 v185, v115, 0x43000000, v198
	v_fmamk_f32 v186, v116, 0x43000000, v198
	v_fmamk_f32 v187, v117, 0x43000000, v198
	v_med3_f32 v180, v180, s69, v199
	v_med3_f32 v181, v181, s69, v199
	v_med3_f32 v182, v182, s69, v199
	v_med3_f32 v183, v183, s69, v199
	v_med3_f32 v184, v184, s69, v199
	v_med3_f32 v185, v185, s69, v199
	v_med3_f32 v186, v186, s69, v199
	v_med3_f32 v187, v187, s69, v199
	v_cvt_i32_f32_e32 v180, v180
	v_cvt_i32_f32_e32 v181, v181
	v_cvt_i32_f32_e32 v182, v182
	v_cvt_i32_f32_e32 v183, v183
	v_cvt_i32_f32_e32 v184, v184
	v_cvt_i32_f32_e32 v185, v185
	v_cvt_i32_f32_e32 v186, v186
	v_cvt_i32_f32_e32 v187, v187
	ds_read_u8 v180, v180
	ds_read_u8 v181, v181
	ds_read_u8 v182, v182
	ds_read_u8 v183, v183
	ds_read_u8 v184, v184
	ds_read_u8 v185, v185
	ds_read_u8 v186, v186
	ds_read_u8 v187, v187
	s_waitcnt lgkmcnt(8)
	v_lshl_or_b32 v132, v133, 8, v132
	v_lshl_or_b32 v134, v135, 8, v134
	v_lshl_or_b32 v136, v137, 8, v136
	v_lshl_or_b32 v169, v170, 8, v169
	v_lshl_or_b32 v132, v134, 16, v132
	v_lshl_or_b32 v133, v169, 16, v136
	global_store_dwordx2 v[130:131], v[132:133], off
	v_fmamk_f32 v132, v110, 0x43000000, v198
	v_fmamk_f32 v133, v111, 0x43000000, v198
	v_fmamk_f32 v134, v112, 0x43000000, v198
	v_fmamk_f32 v135, v113, 0x43000000, v198
	v_fmamk_f32 v136, v106, 0x43000000, v198
	v_fmamk_f32 v137, v107, 0x43000000, v198
	v_fmamk_f32 v169, v108, 0x43000000, v198
	v_fmamk_f32 v170, v109, 0x43000000, v198
	v_med3_f32 v132, v132, s69, v199
	v_med3_f32 v133, v133, s69, v199
	v_med3_f32 v134, v134, s69, v199
	v_med3_f32 v135, v135, s69, v199
	v_med3_f32 v136, v136, s69, v199
	v_med3_f32 v137, v137, s69, v199
	v_med3_f32 v169, v169, s69, v199
	v_med3_f32 v170, v170, s69, v199
	v_cvt_i32_f32_e32 v132, v132
	v_cvt_i32_f32_e32 v133, v133
	v_cvt_i32_f32_e32 v134, v134
	v_cvt_i32_f32_e32 v135, v135
	v_cvt_i32_f32_e32 v136, v136
	v_cvt_i32_f32_e32 v137, v137
	v_cvt_i32_f32_e32 v169, v169
	v_cvt_i32_f32_e32 v170, v170
	ds_read_u8 v132, v132
	ds_read_u8 v133, v133
	ds_read_u8 v134, v134
	ds_read_u8 v135, v135
	ds_read_u8 v136, v136
	ds_read_u8 v137, v137
	ds_read_u8 v169, v169
	ds_read_u8 v170, v170
	s_waitcnt lgkmcnt(8)
	v_lshl_or_b32 v180, v181, 8, v180
	v_lshl_or_b32 v182, v183, 8, v182
	v_lshl_or_b32 v184, v185, 8, v184
	v_lshl_or_b32 v186, v187, 8, v186
	v_lshl_or_b32 v180, v182, 16, v180
	v_lshl_or_b32 v181, v186, 16, v184
	global_store_dwordx2 v[130:131], v[180:181], off offset:128
	v_add_co_u32_e32 v130, vcc, 0x8000, v130
	s_nop 1
	v_addc_co_u32_e32 v131, vcc, 0, v131, vcc
	v_fmamk_f32 v180, v102, 0x43000000, v198
	v_fmamk_f32 v181, v103, 0x43000000, v198
	v_fmamk_f32 v182, v104, 0x43000000, v198
	v_fmamk_f32 v183, v105, 0x43000000, v198
	v_fmamk_f32 v184, v98, 0x43000000, v198
	v_fmamk_f32 v185, v99, 0x43000000, v198
	v_fmamk_f32 v186, v100, 0x43000000, v198
	v_fmamk_f32 v187, v101, 0x43000000, v198
	v_med3_f32 v180, v180, s69, v199
	v_med3_f32 v181, v181, s69, v199
	v_med3_f32 v182, v182, s69, v199
	v_med3_f32 v183, v183, s69, v199
	v_med3_f32 v184, v184, s69, v199
	v_med3_f32 v185, v185, s69, v199
	v_med3_f32 v186, v186, s69, v199
	v_med3_f32 v187, v187, s69, v199
	v_cvt_i32_f32_e32 v180, v180
	v_cvt_i32_f32_e32 v181, v181
	v_cvt_i32_f32_e32 v182, v182
	v_cvt_i32_f32_e32 v183, v183
	v_cvt_i32_f32_e32 v184, v184
	v_cvt_i32_f32_e32 v185, v185
	v_cvt_i32_f32_e32 v186, v186
	v_cvt_i32_f32_e32 v187, v187
	ds_read_u8 v180, v180
	ds_read_u8 v181, v181
	ds_read_u8 v182, v182
	ds_read_u8 v183, v183
	ds_read_u8 v184, v184
	ds_read_u8 v185, v185
	ds_read_u8 v186, v186
	ds_read_u8 v187, v187
	s_waitcnt lgkmcnt(8)
	v_lshl_or_b32 v132, v133, 8, v132
	v_lshl_or_b32 v134, v135, 8, v134
	v_lshl_or_b32 v136, v137, 8, v136
	v_lshl_or_b32 v169, v170, 8, v169
	v_lshl_or_b32 v132, v134, 16, v132
	v_lshl_or_b32 v133, v169, 16, v136
	global_store_dwordx2 v[130:131], v[132:133], off
	v_fmamk_f32 v132, v94, 0x43000000, v198
	v_fmamk_f32 v133, v95, 0x43000000, v198
	v_fmamk_f32 v134, v96, 0x43000000, v198
	v_fmamk_f32 v135, v97, 0x43000000, v198
	v_fmamk_f32 v136, v90, 0x43000000, v198
	v_fmamk_f32 v137, v91, 0x43000000, v198
	v_fmamk_f32 v169, v92, 0x43000000, v198
	v_fmamk_f32 v170, v93, 0x43000000, v198
	v_med3_f32 v132, v132, s69, v199
	v_med3_f32 v133, v133, s69, v199
	v_med3_f32 v134, v134, s69, v199
	v_med3_f32 v135, v135, s69, v199
	v_med3_f32 v136, v136, s69, v199
	v_med3_f32 v137, v137, s69, v199
	v_med3_f32 v169, v169, s69, v199
	v_med3_f32 v170, v170, s69, v199
	v_cvt_i32_f32_e32 v132, v132
	v_cvt_i32_f32_e32 v133, v133
	v_cvt_i32_f32_e32 v134, v134
	v_cvt_i32_f32_e32 v135, v135
	v_cvt_i32_f32_e32 v136, v136
	v_cvt_i32_f32_e32 v137, v137
	v_cvt_i32_f32_e32 v169, v169
	v_cvt_i32_f32_e32 v170, v170
	ds_read_u8 v132, v132
	ds_read_u8 v133, v133
	ds_read_u8 v134, v134
	ds_read_u8 v135, v135
	ds_read_u8 v136, v136
	ds_read_u8 v137, v137
	ds_read_u8 v169, v169
	ds_read_u8 v170, v170
	s_waitcnt lgkmcnt(8)
	v_lshl_or_b32 v180, v181, 8, v180
	v_lshl_or_b32 v182, v183, 8, v182
	v_lshl_or_b32 v184, v185, 8, v184
	v_lshl_or_b32 v186, v187, 8, v186
	v_lshl_or_b32 v180, v182, 16, v180
	v_lshl_or_b32 v181, v186, 16, v184
	global_store_dwordx2 v[130:131], v[180:181], off offset:128
	v_add_co_u32_e32 v130, vcc, 0x8000, v130
	s_nop 1
	v_addc_co_u32_e32 v131, vcc, 0, v131, vcc
	v_fmamk_f32 v180, v86, 0x43000000, v198
	v_fmamk_f32 v181, v87, 0x43000000, v198
	v_fmamk_f32 v182, v88, 0x43000000, v198
	v_fmamk_f32 v183, v89, 0x43000000, v198
	v_fmamk_f32 v184, v82, 0x43000000, v198
	v_fmamk_f32 v185, v83, 0x43000000, v198
	v_fmamk_f32 v186, v84, 0x43000000, v198
	v_fmamk_f32 v187, v85, 0x43000000, v198
	v_med3_f32 v180, v180, s69, v199
	v_med3_f32 v181, v181, s69, v199
	v_med3_f32 v182, v182, s69, v199
	v_med3_f32 v183, v183, s69, v199
	v_med3_f32 v184, v184, s69, v199
	v_med3_f32 v185, v185, s69, v199
	v_med3_f32 v186, v186, s69, v199
	v_med3_f32 v187, v187, s69, v199
	v_cvt_i32_f32_e32 v180, v180
	v_cvt_i32_f32_e32 v181, v181
	v_cvt_i32_f32_e32 v182, v182
	v_cvt_i32_f32_e32 v183, v183
	v_cvt_i32_f32_e32 v184, v184
	v_cvt_i32_f32_e32 v185, v185
	v_cvt_i32_f32_e32 v186, v186
	v_cvt_i32_f32_e32 v187, v187
	ds_read_u8 v180, v180
	ds_read_u8 v181, v181
	ds_read_u8 v182, v182
	ds_read_u8 v183, v183
	ds_read_u8 v184, v184
	ds_read_u8 v185, v185
	ds_read_u8 v186, v186
	ds_read_u8 v187, v187
	s_waitcnt lgkmcnt(8)
	v_lshl_or_b32 v132, v133, 8, v132
	v_lshl_or_b32 v134, v135, 8, v134
	v_lshl_or_b32 v136, v137, 8, v136
	v_lshl_or_b32 v169, v170, 8, v169
	v_lshl_or_b32 v132, v134, 16, v132
	v_lshl_or_b32 v133, v169, 16, v136
	global_store_dwordx2 v[130:131], v[132:133], off
	v_fmamk_f32 v132, v78, 0x43000000, v198
	v_fmamk_f32 v133, v79, 0x43000000, v198
	v_fmamk_f32 v134, v80, 0x43000000, v198
	v_fmamk_f32 v135, v81, 0x43000000, v198
	v_fmamk_f32 v136, v74, 0x43000000, v198
	v_fmamk_f32 v137, v75, 0x43000000, v198
	v_fmamk_f32 v169, v76, 0x43000000, v198
	v_fmamk_f32 v170, v77, 0x43000000, v198
	v_med3_f32 v132, v132, s69, v199
	v_med3_f32 v133, v133, s69, v199
	v_med3_f32 v134, v134, s69, v199
	v_med3_f32 v135, v135, s69, v199
	v_med3_f32 v136, v136, s69, v199
	v_med3_f32 v137, v137, s69, v199
	v_med3_f32 v169, v169, s69, v199
	v_med3_f32 v170, v170, s69, v199
	v_cvt_i32_f32_e32 v132, v132
	v_cvt_i32_f32_e32 v133, v133
	v_cvt_i32_f32_e32 v134, v134
	v_cvt_i32_f32_e32 v135, v135
	v_cvt_i32_f32_e32 v136, v136
	v_cvt_i32_f32_e32 v137, v137
	v_cvt_i32_f32_e32 v169, v169
	v_cvt_i32_f32_e32 v170, v170
	ds_read_u8 v132, v132
	ds_read_u8 v133, v133
	ds_read_u8 v134, v134
	ds_read_u8 v135, v135
	ds_read_u8 v136, v136
	ds_read_u8 v137, v137
	ds_read_u8 v169, v169
	ds_read_u8 v170, v170
	s_waitcnt lgkmcnt(8)
	v_lshl_or_b32 v180, v181, 8, v180
	v_lshl_or_b32 v182, v183, 8, v182
	v_lshl_or_b32 v184, v185, 8, v184
	v_lshl_or_b32 v186, v187, 8, v186
	v_lshl_or_b32 v180, v182, 16, v180
	v_lshl_or_b32 v181, v186, 16, v184
	global_store_dwordx2 v[130:131], v[180:181], off offset:128
	v_add_co_u32_e32 v130, vcc, 0x8000, v130
	s_nop 1
	v_addc_co_u32_e32 v131, vcc, 0, v131, vcc
	v_fmamk_f32 v180, v70, 0x43000000, v198
	v_fmamk_f32 v181, v71, 0x43000000, v198
	v_fmamk_f32 v182, v72, 0x43000000, v198
	v_fmamk_f32 v183, v73, 0x43000000, v198
	v_fmamk_f32 v184, v66, 0x43000000, v198
	v_fmamk_f32 v185, v67, 0x43000000, v198
	v_fmamk_f32 v186, v68, 0x43000000, v198
	v_fmamk_f32 v187, v69, 0x43000000, v198
	v_med3_f32 v180, v180, s69, v199
	v_med3_f32 v181, v181, s69, v199
	v_med3_f32 v182, v182, s69, v199
	v_med3_f32 v183, v183, s69, v199
	v_med3_f32 v184, v184, s69, v199
	v_med3_f32 v185, v185, s69, v199
	v_med3_f32 v186, v186, s69, v199
	v_med3_f32 v187, v187, s69, v199
	v_cvt_i32_f32_e32 v180, v180
	v_cvt_i32_f32_e32 v181, v181
	v_cvt_i32_f32_e32 v182, v182
	v_cvt_i32_f32_e32 v183, v183
	v_cvt_i32_f32_e32 v184, v184
	v_cvt_i32_f32_e32 v185, v185
	v_cvt_i32_f32_e32 v186, v186
	v_cvt_i32_f32_e32 v187, v187
	ds_read_u8 v180, v180
	ds_read_u8 v181, v181
	ds_read_u8 v182, v182
	ds_read_u8 v183, v183
	ds_read_u8 v184, v184
	ds_read_u8 v185, v185
	ds_read_u8 v186, v186
	ds_read_u8 v187, v187
	s_waitcnt lgkmcnt(8)
	v_lshl_or_b32 v132, v133, 8, v132
	v_lshl_or_b32 v134, v135, 8, v134
	v_lshl_or_b32 v136, v137, 8, v136
	v_lshl_or_b32 v169, v170, 8, v169
	v_lshl_or_b32 v132, v134, 16, v132
	v_lshl_or_b32 v133, v169, 16, v136
	global_store_dwordx2 v[130:131], v[132:133], off
	v_fmamk_f32 v132, v62, 0x43000000, v198
	v_fmamk_f32 v133, v63, 0x43000000, v198
	v_fmamk_f32 v134, v64, 0x43000000, v198
	v_fmamk_f32 v135, v65, 0x43000000, v198
	v_fmamk_f32 v136, v58, 0x43000000, v198
	v_fmamk_f32 v137, v59, 0x43000000, v198
	v_fmamk_f32 v169, v60, 0x43000000, v198
	v_fmamk_f32 v170, v61, 0x43000000, v198
	v_med3_f32 v132, v132, s69, v199
	v_med3_f32 v133, v133, s69, v199
	v_med3_f32 v134, v134, s69, v199
	v_med3_f32 v135, v135, s69, v199
	v_med3_f32 v136, v136, s69, v199
	v_med3_f32 v137, v137, s69, v199
	v_med3_f32 v169, v169, s69, v199
	v_med3_f32 v170, v170, s69, v199
	v_cvt_i32_f32_e32 v132, v132
	v_cvt_i32_f32_e32 v133, v133
	v_cvt_i32_f32_e32 v134, v134
	v_cvt_i32_f32_e32 v135, v135
	v_cvt_i32_f32_e32 v136, v136
	v_cvt_i32_f32_e32 v137, v137
	v_cvt_i32_f32_e32 v169, v169
	v_cvt_i32_f32_e32 v170, v170
	ds_read_u8 v132, v132
	ds_read_u8 v133, v133
	ds_read_u8 v134, v134
	ds_read_u8 v135, v135
	ds_read_u8 v136, v136
	ds_read_u8 v137, v137
	ds_read_u8 v169, v169
	ds_read_u8 v170, v170
	s_waitcnt lgkmcnt(8)
	v_lshl_or_b32 v180, v181, 8, v180
	v_lshl_or_b32 v182, v183, 8, v182
	v_lshl_or_b32 v184, v185, 8, v184
	v_lshl_or_b32 v186, v187, 8, v186
	v_lshl_or_b32 v180, v182, 16, v180
	v_lshl_or_b32 v181, v186, 16, v184
	global_store_dwordx2 v[130:131], v[180:181], off offset:128
	v_add_co_u32_e32 v130, vcc, 0x28000, v130
	s_nop 1
	v_addc_co_u32_e32 v131, vcc, 0, v131, vcc
	v_fmamk_f32 v180, v54, 0x43000000, v198
	v_fmamk_f32 v181, v55, 0x43000000, v198
	v_fmamk_f32 v182, v56, 0x43000000, v198
	v_fmamk_f32 v183, v57, 0x43000000, v198
	v_fmamk_f32 v184, v50, 0x43000000, v198
	v_fmamk_f32 v185, v51, 0x43000000, v198
	v_fmamk_f32 v186, v52, 0x43000000, v198
	v_fmamk_f32 v187, v53, 0x43000000, v198
	v_med3_f32 v180, v180, s69, v199
	v_med3_f32 v181, v181, s69, v199
	v_med3_f32 v182, v182, s69, v199
	v_med3_f32 v183, v183, s69, v199
	v_med3_f32 v184, v184, s69, v199
	v_med3_f32 v185, v185, s69, v199
	v_med3_f32 v186, v186, s69, v199
	v_med3_f32 v187, v187, s69, v199
	v_cvt_i32_f32_e32 v180, v180
	v_cvt_i32_f32_e32 v181, v181
	v_cvt_i32_f32_e32 v182, v182
	v_cvt_i32_f32_e32 v183, v183
	v_cvt_i32_f32_e32 v184, v184
	v_cvt_i32_f32_e32 v185, v185
	v_cvt_i32_f32_e32 v186, v186
	v_cvt_i32_f32_e32 v187, v187
	ds_read_u8 v180, v180
	ds_read_u8 v181, v181
	ds_read_u8 v182, v182
	ds_read_u8 v183, v183
	ds_read_u8 v184, v184
	ds_read_u8 v185, v185
	ds_read_u8 v186, v186
	ds_read_u8 v187, v187
	s_waitcnt lgkmcnt(8)
	v_lshl_or_b32 v132, v133, 8, v132
	v_lshl_or_b32 v134, v135, 8, v134
	v_lshl_or_b32 v136, v137, 8, v136
	v_lshl_or_b32 v169, v170, 8, v169
	v_lshl_or_b32 v132, v134, 16, v132
	v_lshl_or_b32 v133, v169, 16, v136
	global_store_dwordx2 v[130:131], v[132:133], off
	v_fmamk_f32 v132, v46, 0x43000000, v198
	v_fmamk_f32 v133, v47, 0x43000000, v198
	v_fmamk_f32 v134, v48, 0x43000000, v198
	v_fmamk_f32 v135, v49, 0x43000000, v198
	v_fmamk_f32 v136, v42, 0x43000000, v198
	v_fmamk_f32 v137, v43, 0x43000000, v198
	v_fmamk_f32 v169, v44, 0x43000000, v198
	v_fmamk_f32 v170, v45, 0x43000000, v198
	v_med3_f32 v132, v132, s69, v199
	v_med3_f32 v133, v133, s69, v199
	v_med3_f32 v134, v134, s69, v199
	v_med3_f32 v135, v135, s69, v199
	v_med3_f32 v136, v136, s69, v199
	v_med3_f32 v137, v137, s69, v199
	v_med3_f32 v169, v169, s69, v199
	v_med3_f32 v170, v170, s69, v199
	v_cvt_i32_f32_e32 v132, v132
	v_cvt_i32_f32_e32 v133, v133
	v_cvt_i32_f32_e32 v134, v134
	v_cvt_i32_f32_e32 v135, v135
	v_cvt_i32_f32_e32 v136, v136
	v_cvt_i32_f32_e32 v137, v137
	v_cvt_i32_f32_e32 v169, v169
	v_cvt_i32_f32_e32 v170, v170
	ds_read_u8 v132, v132
	ds_read_u8 v133, v133
	ds_read_u8 v134, v134
	ds_read_u8 v135, v135
	ds_read_u8 v136, v136
	ds_read_u8 v137, v137
	ds_read_u8 v169, v169
	ds_read_u8 v170, v170
	s_waitcnt lgkmcnt(8)
	v_lshl_or_b32 v180, v181, 8, v180
	v_lshl_or_b32 v182, v183, 8, v182
	v_lshl_or_b32 v184, v185, 8, v184
	v_lshl_or_b32 v186, v187, 8, v186
	v_lshl_or_b32 v180, v182, 16, v180
	v_lshl_or_b32 v181, v186, 16, v184
	global_store_dwordx2 v[130:131], v[180:181], off offset:128
	v_add_co_u32_e32 v130, vcc, 0x8000, v130
	s_nop 1
	v_addc_co_u32_e32 v131, vcc, 0, v131, vcc
	v_fmamk_f32 v180, v38, 0x43000000, v198
	v_fmamk_f32 v181, v39, 0x43000000, v198
	v_fmamk_f32 v182, v40, 0x43000000, v198
	v_fmamk_f32 v183, v41, 0x43000000, v198
	v_fmamk_f32 v184, v34, 0x43000000, v198
	v_fmamk_f32 v185, v35, 0x43000000, v198
	v_fmamk_f32 v186, v36, 0x43000000, v198
	v_fmamk_f32 v187, v37, 0x43000000, v198
	v_med3_f32 v180, v180, s69, v199
	v_med3_f32 v181, v181, s69, v199
	v_med3_f32 v182, v182, s69, v199
	v_med3_f32 v183, v183, s69, v199
	v_med3_f32 v184, v184, s69, v199
	v_med3_f32 v185, v185, s69, v199
	v_med3_f32 v186, v186, s69, v199
	v_med3_f32 v187, v187, s69, v199
	v_cvt_i32_f32_e32 v180, v180
	v_cvt_i32_f32_e32 v181, v181
	v_cvt_i32_f32_e32 v182, v182
	v_cvt_i32_f32_e32 v183, v183
	v_cvt_i32_f32_e32 v184, v184
	v_cvt_i32_f32_e32 v185, v185
	v_cvt_i32_f32_e32 v186, v186
	v_cvt_i32_f32_e32 v187, v187
	ds_read_u8 v180, v180
	ds_read_u8 v181, v181
	ds_read_u8 v182, v182
	ds_read_u8 v183, v183
	ds_read_u8 v184, v184
	ds_read_u8 v185, v185
	ds_read_u8 v186, v186
	ds_read_u8 v187, v187
	s_waitcnt lgkmcnt(8)
	v_lshl_or_b32 v132, v133, 8, v132
	v_lshl_or_b32 v134, v135, 8, v134
	v_lshl_or_b32 v136, v137, 8, v136
	v_lshl_or_b32 v169, v170, 8, v169
	v_lshl_or_b32 v132, v134, 16, v132
	v_lshl_or_b32 v133, v169, 16, v136
	global_store_dwordx2 v[130:131], v[132:133], off
	v_fmamk_f32 v132, v30, 0x43000000, v198
	v_fmamk_f32 v133, v31, 0x43000000, v198
	v_fmamk_f32 v134, v32, 0x43000000, v198
	v_fmamk_f32 v135, v33, 0x43000000, v198
	v_fmamk_f32 v136, v26, 0x43000000, v198
	v_fmamk_f32 v137, v27, 0x43000000, v198
	v_fmamk_f32 v169, v28, 0x43000000, v198
	v_fmamk_f32 v170, v29, 0x43000000, v198
	v_med3_f32 v132, v132, s69, v199
	v_med3_f32 v133, v133, s69, v199
	v_med3_f32 v134, v134, s69, v199
	v_med3_f32 v135, v135, s69, v199
	v_med3_f32 v136, v136, s69, v199
	v_med3_f32 v137, v137, s69, v199
	v_med3_f32 v169, v169, s69, v199
	v_med3_f32 v170, v170, s69, v199
	v_cvt_i32_f32_e32 v132, v132
	v_cvt_i32_f32_e32 v133, v133
	v_cvt_i32_f32_e32 v134, v134
	v_cvt_i32_f32_e32 v135, v135
	v_cvt_i32_f32_e32 v136, v136
	v_cvt_i32_f32_e32 v137, v137
	v_cvt_i32_f32_e32 v169, v169
	v_cvt_i32_f32_e32 v170, v170
	ds_read_u8 v132, v132
	ds_read_u8 v133, v133
	ds_read_u8 v134, v134
	ds_read_u8 v135, v135
	ds_read_u8 v136, v136
	ds_read_u8 v137, v137
	ds_read_u8 v169, v169
	ds_read_u8 v170, v170
	s_waitcnt lgkmcnt(8)
	v_lshl_or_b32 v180, v181, 8, v180
	v_lshl_or_b32 v182, v183, 8, v182
	v_lshl_or_b32 v184, v185, 8, v184
	v_lshl_or_b32 v186, v187, 8, v186
	v_lshl_or_b32 v180, v182, 16, v180
	v_lshl_or_b32 v181, v186, 16, v184
	global_store_dwordx2 v[130:131], v[180:181], off offset:128
	v_add_co_u32_e32 v130, vcc, 0x8000, v130
	s_nop 1
	v_addc_co_u32_e32 v131, vcc, 0, v131, vcc
	v_fmamk_f32 v180, v22, 0x43000000, v198
	v_fmamk_f32 v181, v23, 0x43000000, v198
	v_fmamk_f32 v182, v24, 0x43000000, v198
	v_fmamk_f32 v183, v25, 0x43000000, v198
	v_fmamk_f32 v184, v18, 0x43000000, v198
	v_fmamk_f32 v185, v19, 0x43000000, v198
	v_fmamk_f32 v186, v20, 0x43000000, v198
	v_fmamk_f32 v187, v21, 0x43000000, v198
	v_med3_f32 v180, v180, s69, v199
	v_med3_f32 v181, v181, s69, v199
	v_med3_f32 v182, v182, s69, v199
	v_med3_f32 v183, v183, s69, v199
	v_med3_f32 v184, v184, s69, v199
	v_med3_f32 v185, v185, s69, v199
	v_med3_f32 v186, v186, s69, v199
	v_med3_f32 v187, v187, s69, v199
	v_cvt_i32_f32_e32 v180, v180
	v_cvt_i32_f32_e32 v181, v181
	v_cvt_i32_f32_e32 v182, v182
	v_cvt_i32_f32_e32 v183, v183
	v_cvt_i32_f32_e32 v184, v184
	v_cvt_i32_f32_e32 v185, v185
	v_cvt_i32_f32_e32 v186, v186
	v_cvt_i32_f32_e32 v187, v187
	ds_read_u8 v180, v180
	ds_read_u8 v181, v181
	ds_read_u8 v182, v182
	ds_read_u8 v183, v183
	ds_read_u8 v184, v184
	ds_read_u8 v185, v185
	ds_read_u8 v186, v186
	ds_read_u8 v187, v187
	s_waitcnt lgkmcnt(8)
	v_lshl_or_b32 v132, v133, 8, v132
	v_lshl_or_b32 v134, v135, 8, v134
	v_lshl_or_b32 v136, v137, 8, v136
	v_lshl_or_b32 v169, v170, 8, v169
	v_lshl_or_b32 v132, v134, 16, v132
	v_lshl_or_b32 v133, v169, 16, v136
	global_store_dwordx2 v[130:131], v[132:133], off
	v_fmamk_f32 v132, v14, 0x43000000, v198
	v_fmamk_f32 v133, v15, 0x43000000, v198
	v_fmamk_f32 v134, v16, 0x43000000, v198
	v_fmamk_f32 v135, v17, 0x43000000, v198
	v_fmamk_f32 v136, v10, 0x43000000, v198
	v_fmamk_f32 v137, v11, 0x43000000, v198
	v_fmamk_f32 v169, v12, 0x43000000, v198
	v_fmamk_f32 v170, v13, 0x43000000, v198
	v_med3_f32 v132, v132, s69, v199
	v_med3_f32 v133, v133, s69, v199
	v_med3_f32 v134, v134, s69, v199
	v_med3_f32 v135, v135, s69, v199
	v_med3_f32 v136, v136, s69, v199
	v_med3_f32 v137, v137, s69, v199
	v_med3_f32 v169, v169, s69, v199
	v_med3_f32 v170, v170, s69, v199
	v_cvt_i32_f32_e32 v132, v132
	v_cvt_i32_f32_e32 v133, v133
	v_cvt_i32_f32_e32 v134, v134
	v_cvt_i32_f32_e32 v135, v135
	v_cvt_i32_f32_e32 v136, v136
	v_cvt_i32_f32_e32 v137, v137
	v_cvt_i32_f32_e32 v169, v169
	v_cvt_i32_f32_e32 v170, v170
	ds_read_u8 v132, v132
	ds_read_u8 v133, v133
	ds_read_u8 v134, v134
	ds_read_u8 v135, v135
	ds_read_u8 v136, v136
	ds_read_u8 v137, v137
	ds_read_u8 v169, v169
	ds_read_u8 v170, v170
	s_waitcnt lgkmcnt(8)
	v_lshl_or_b32 v180, v181, 8, v180
	v_lshl_or_b32 v182, v183, 8, v182
	v_lshl_or_b32 v184, v185, 8, v184
	v_lshl_or_b32 v186, v187, 8, v186
	v_lshl_or_b32 v180, v182, 16, v180
	v_lshl_or_b32 v181, v186, 16, v184
	global_store_dwordx2 v[130:131], v[180:181], off offset:128
	v_add_co_u32_e32 v130, vcc, 0x8000, v130
	s_nop 1
	v_addc_co_u32_e32 v131, vcc, 0, v131, vcc
	v_fmamk_f32 v180, v6, 0x43000000, v198
	v_fmamk_f32 v181, v7, 0x43000000, v198
	v_fmamk_f32 v182, v8, 0x43000000, v198
	v_fmamk_f32 v183, v9, 0x43000000, v198
	v_fmamk_f32 v184, v2, 0x43000000, v198
	v_fmamk_f32 v185, v3, 0x43000000, v198
	v_fmamk_f32 v186, v4, 0x43000000, v198
	v_fmamk_f32 v187, v5, 0x43000000, v198
	v_med3_f32 v180, v180, s69, v199
	v_med3_f32 v181, v181, s69, v199
	v_med3_f32 v182, v182, s69, v199
	v_med3_f32 v183, v183, s69, v199
	v_med3_f32 v184, v184, s69, v199
	v_med3_f32 v185, v185, s69, v199
	v_med3_f32 v186, v186, s69, v199
	v_med3_f32 v187, v187, s69, v199
	v_cvt_i32_f32_e32 v180, v180
	v_cvt_i32_f32_e32 v181, v181
	v_cvt_i32_f32_e32 v182, v182
	v_cvt_i32_f32_e32 v183, v183
	v_cvt_i32_f32_e32 v184, v184
	v_cvt_i32_f32_e32 v185, v185
	v_cvt_i32_f32_e32 v186, v186
	v_cvt_i32_f32_e32 v187, v187
	ds_read_u8 v180, v180
	ds_read_u8 v181, v181
	ds_read_u8 v182, v182
	ds_read_u8 v183, v183
	ds_read_u8 v184, v184
	ds_read_u8 v185, v185
	ds_read_u8 v186, v186
	ds_read_u8 v187, v187
	s_waitcnt lgkmcnt(8)
	v_lshl_or_b32 v132, v133, 8, v132
	v_lshl_or_b32 v134, v135, 8, v134
	v_lshl_or_b32 v136, v137, 8, v136
	v_lshl_or_b32 v169, v170, 8, v169
	v_lshl_or_b32 v132, v134, 16, v132
	v_lshl_or_b32 v133, v169, 16, v136
	global_store_dwordx2 v[130:131], v[132:133], off
	s_waitcnt lgkmcnt(0)
	v_lshl_or_b32 v180, v181, 8, v180
	v_lshl_or_b32 v182, v183, 8, v182
	v_lshl_or_b32 v184, v185, 8, v184
	v_lshl_or_b32 v186, v187, 8, v186
	v_lshl_or_b32 v180, v182, 16, v180
	v_lshl_or_b32 v181, v186, 16, v184
	global_store_dwordx2 v[130:131], v[180:181], off offset:128
	s_mov_b64 s[10:11], 0
